# hybrid K1 ring 16 with 16 of 18 chunks private (1/9 of the matrix in the queues) + last-chunk early flush
# baseline (speedup 1.0000x reference)
.Lk1_scan:
	s_load_dwordx2 s[4:5], s[0:1], 0x0
	s_load_dwordx4 s[8:11], s[0:1], 0x20
	s_load_dwordx2 s[12:13], s[0:1], 0x30
	v_and_b32_e32 v6, 63, v0
	v_readfirstlane_b32 s3, v0
	v_lshlrev_b32_e32 v1, 4, v6
	v_lshlrev_b32_e32 v2, 2, v6
	v_or_b32_e32 v3, 1, v2
	v_or_b32_e32 v4, 2, v2
	v_or_b32_e32 v5, 3, v2
	s_lshr_b32 s3, s3, 6
	s_sub_u32 s16, s2, 0x60
	s_lshl_b32 s16, s16, 2
	s_add_u32 s16, s16, s3
	s_mul_i32 s17, s16, 0x48000
	s_lshr_b32 s18, s17, 2
	s_lshl_b32 s24, s3, 13
	s_mov_b32 s25, s24
	s_mov_b32 s28, s24
	s_mov_b32 s36, 0
	s_mov_b64 s[62:63], 0
	v_mov_b32_e32 v21, 1
	s_mov_b32 s27, 0
	s_mov_b32 s29, 0x55555556
	s_mov_b32 s31, 0xc0000
	s_waitcnt lgkmcnt(0)
	s_and_b32 s50, s16, 15
	s_mul_i32 s52, s50, 256
	s_add_u32 s52, s52, 32768
	s_lshl_b32 s53, s50, 6
	s_add_u32 s53, s53, 0xe000
	s_add_u32 s54, s10, s53
	s_addc_u32 s55, s11, 0
	s_mul_i32 s59, s16, 16
	s_mul_i32 s57, s59, 0x4000
	s_lshr_b32 s18, s57, 2
	s_add_u32 s6, s4, s57
	s_addc_u32 s7, s5, 0
	v_mov_b32_e32 v27, 0
	global_load_dwordx4 v[28:31], v1, s[6:7] nt
	s_add_u32 s6, s6, 0x400
	s_addc_u32 s7, s7, 0
	global_load_dwordx4 v[32:35], v1, s[6:7] nt
	s_add_u32 s6, s6, 0x400
	s_addc_u32 s7, s7, 0
	global_load_dwordx4 v[36:39], v1, s[6:7] nt
	s_add_u32 s6, s6, 0x400
	s_addc_u32 s7, s7, 0
	global_load_dwordx4 v[40:43], v1, s[6:7] nt
	s_add_u32 s6, s6, 0x400
	s_addc_u32 s7, s7, 0
	global_load_dwordx4 v[44:47], v1, s[6:7] nt
	s_add_u32 s6, s6, 0x400
	s_addc_u32 s7, s7, 0
	global_load_dwordx4 v[48:51], v1, s[6:7] nt
	s_add_u32 s6, s6, 0x400
	s_addc_u32 s7, s7, 0
	global_load_dwordx4 v[52:55], v1, s[6:7] nt
	s_add_u32 s6, s6, 0x400
	s_addc_u32 s7, s7, 0
	global_load_dwordx4 v[56:59], v1, s[6:7] nt
	s_add_u32 s6, s6, 0x400
	s_addc_u32 s7, s7, 0
	global_load_dwordx4 v[60:63], v1, s[6:7] nt
	s_add_u32 s6, s6, 0x400
	s_addc_u32 s7, s7, 0
	global_load_dwordx4 v[64:67], v1, s[6:7] nt
	s_add_u32 s6, s6, 0x400
	s_addc_u32 s7, s7, 0
	global_load_dwordx4 v[68:71], v1, s[6:7] nt
	s_add_u32 s6, s6, 0x400
	s_addc_u32 s7, s7, 0
	global_load_dwordx4 v[72:75], v1, s[6:7] nt
	s_add_u32 s6, s6, 0x400
	s_addc_u32 s7, s7, 0
	global_load_dwordx4 v[76:79], v1, s[6:7] nt
	s_add_u32 s6, s6, 0x400
	s_addc_u32 s7, s7, 0
	global_load_dwordx4 v[80:83], v1, s[6:7] nt
	s_add_u32 s6, s6, 0x400
	s_addc_u32 s7, s7, 0
	global_load_dwordx4 v[84:87], v1, s[6:7] nt
	s_add_u32 s6, s6, 0x400
	s_addc_u32 s7, s7, 0
	global_load_dwordx4 v[88:91], v1, s[6:7] nt
	s_add_u32 s6, s6, 0x400
	s_addc_u32 s7, s7, 0
	s_mov_b32 s26, 18
	s_add_u32 s57, s59, 1
	s_mul_i32 s57, s57, 0x4000
	s_lshr_b32 s58, s57, 2
	s_add_u32 s6, s4, s57
	s_addc_u32 s7, s5, 0
	s_mov_b32 s26, 0

.Lk1_contm_15:
	global_load_dwordx4 v[60:63], v1, s[6:7] nt
	s_add_u32 s6, s6, 0x400
	s_addc_u32 s7, s7, 0
	global_load_dwordx4 v[64:67], v1, s[6:7] nt
	s_add_u32 s6, s6, 0x400
	s_addc_u32 s7, s7, 0
	global_load_dwordx4 v[68:71], v1, s[6:7] nt
	s_add_u32 s6, s6, 0x400
	s_addc_u32 s7, s7, 0
	global_load_dwordx4 v[72:75], v1, s[6:7] nt
	s_add_u32 s6, s6, 0x400
	s_addc_u32 s7, s7, 0
	global_load_dwordx4 v[76:79], v1, s[6:7] nt
	s_add_u32 s6, s6, 0x400
	s_addc_u32 s7, s7, 0
	global_load_dwordx4 v[80:83], v1, s[6:7] nt
	s_add_u32 s6, s6, 0x400
	s_addc_u32 s7, s7, 0
	global_load_dwordx4 v[84:87], v1, s[6:7] nt
	s_add_u32 s6, s6, 0x400
	s_addc_u32 s7, s7, 0
	global_load_dwordx4 v[88:91], v1, s[6:7] nt
	s_add_u32 s6, s6, 0x400
	s_addc_u32 s7, s7, 0
	s_mov_b32 s18, s58
	s_add_u32 s60, s26, 2
	s_cmp_lt_u32 s60, 16
	s_cbranch_scc0 .Lk1_dynid
	s_add_u32 s57, s59, s60
	s_branch .Lk1_haveid

.Lk1_haveid:
	s_mul_i32 s57, s57, 0x4000
	s_lshr_b32 s58, s57, 2
	s_add_u32 s6, s4, s57
	s_addc_u32 s7, s5, 0
	s_add_u32 s60, s26, 3
	s_cmp_lt_u32 s60, 16
	s_cbranch_scc1 .Lk1_noreq
	s_mov_b64 exec, 1
	global_atomic_add v26, v27, v21, s[54:55] sc0
	s_mov_b64 exec, -1
